# v23 + row_scale_table fast path (256-workgroup grid: one row panel per workgroup, 256 rstd computed once by threads 0-255 with the same summation tree, written to units 0-3) in the w1, G_in(l=1) and K
# speedup vs baseline: 1.0203x; 1.0095x over previous
.LBB0_141:
.LBB0_142:
	s_cmp_eq_u32 s36, 2
	v_readlane_b32 s44, v254, 0
	s_cselect_b64 s[40:41], -1, 0
	s_mov_b64 s[42:43], s[82:83]
	v_readlane_b32 s45, v254, 1
	s_and_b64 s[0:1], s[40:41], exec
	v_mov_b32_e32 v1, v0
	s_cselect_b32 s0, 24, 8
	s_ashr_i32 s45, s44, 31
	s_waitcnt vmcnt(0)
	v_mov_b64_e32 v[2:3], s[44:45]
	s_waitcnt vmcnt(5)
	v_ashrrev_i32_e32 v34, 8, v1
	s_lshl_b32 s24, s0, 5
	s_lshl_b32 s4, s0, 2
	v_mad_i64_i32 v[2:3], s[0:1], v34, s33, v[2:3]
	s_or_b32 s5, s4, 1
	s_cmp_lg_u32 s33, 0x100
	s_cbranch_scc1 .Lrst_spl_slow
	v_cmp_gt_u32_e32 vcc, 0x100, v0
	s_and_saveexec_b64 s[0:1], vcc
	s_cbranch_execz .Lrst_spl_done
	s_and_b32 s8, s44, 7
	s_lshl_b32 s8, s8, 2
	s_bfe_u32 s28, s44, 0x20003
	s_or_b32 s8, s8, s28
	s_lshl_b32 s8, s8, 15
	s_add_u32 s28, s82, 0x36300000
	s_addc_u32 s29, s83, 0
	s_add_u32 s28, s28, s8
	s_addc_u32 s29, s29, 0
	v_lshlrev_b32_e32 v2, 7, v0
	global_load_dwordx4 v[4:7], v2, s[28:29]
	global_load_dwordx4 v[8:11], v2, s[28:29] offset:16
	global_load_dwordx4 v[12:15], v2, s[28:29] offset:32
	global_load_dwordx4 v[16:19], v2, s[28:29] offset:48
	global_load_dwordx4 v[20:23], v2, s[28:29] offset:64
	global_load_dwordx4 v[24:27], v2, s[28:29] offset:80
	global_load_dwordx4 v[28:31], v2, s[28:29] offset:96
	global_load_dwordx4 v[32:35], v2, s[28:29] offset:112
	v_readlane_b32 s8, v255, 4
	v_mov_b32_e32 v36, 0x358637bd
	s_waitcnt vmcnt(0)
	v_pk_add_f32 v[4:5], v[4:5], v[8:9]
	v_pk_add_f32 v[6:7], v[6:7], v[10:11]
	v_pk_add_f32 v[12:13], v[12:13], v[16:17]
	v_pk_add_f32 v[14:15], v[14:15], v[18:19]
	v_pk_add_f32 v[20:21], v[20:21], v[24:25]
	v_pk_add_f32 v[22:23], v[22:23], v[26:27]
	v_pk_add_f32 v[28:29], v[28:29], v[32:33]
	v_pk_add_f32 v[30:31], v[30:31], v[34:35]
	v_pk_add_f32 v[4:5], v[4:5], v[12:13]
	v_pk_add_f32 v[6:7], v[6:7], v[14:15]
	v_pk_add_f32 v[20:21], v[20:21], v[28:29]
	v_pk_add_f32 v[22:23], v[22:23], v[30:31]
	v_pk_add_f32 v[4:5], v[4:5], v[20:21]
	v_pk_add_f32 v[6:7], v[6:7], v[22:23]
	s_nop 0
	v_add_f32_e32 v4, v5, v4
	v_add_f32_e32 v6, v6, v7
	v_add_f32_e32 v4, v4, v6
	v_fmamk_f32 v4, v4, 0x3a000000, v36
	v_rsq_f32_e32 v4, v4
	v_lshl_add_u32 v3, v0, 2, s8
	s_nop 0
	ds_write_b32 v3, v4
	ds_write_b32 v3, v4 offset:1024
	ds_write_b32 v3, v4 offset:2048
	ds_write_b32 v3, v4 offset:3072

.Lrst_spl_slow:
	v_cmp_gt_i64_e32 vcc, s[24:25], v[2:3]
	v_mov_b32_e32 v37, 0
	s_and_saveexec_b64 s[28:29], vcc
	s_cbranch_execz .LBB0_144
	v_ashrrev_i32_e32 v3, 31, v2
	v_lshrrev_b32_e32 v3, 29, v3
	v_add_u32_e32 v3, v2, v3
	s_abs_i32 s8, s4
	v_ashrrev_i32_e32 v4, 3, v3
	v_and_b32_e32 v3, -8, v3
	s_waitcnt lgkmcnt(3)
	v_cvt_f32_u32_e32 v6, s8
	v_sub_u32_e32 v2, v2, v3
	v_mov_b32_e32 v3, s4
	v_mov_b32_e32 v5, s5
	v_cmp_gt_i32_e64 s[0:1], 0, v2
	s_nop 1
	v_cndmask_b32_e64 v3, v3, v5, s[0:1]
	v_mul_lo_u32 v2, v3, v2
	v_rcp_iflag_f32_e32 v3, v6
	s_sub_i32 s0, 0, s8
	v_add_u32_e32 v2, v2, v4
	v_sub_u32_e32 v5, 0, v2
	v_mul_f32_e32 v3, 0x4f7ffffe, v3
	v_cvt_u32_f32_e32 v3, v3
	v_max_i32_e32 v5, v2, v5
	v_xor_b32_e32 v4, s4, v2
	v_ashrrev_i32_e32 v4, 31, v4
	v_mul_lo_u32 v6, s0, v3
	v_mul_hi_u32 v6, v3, v6
	v_add_u32_e32 v3, v3, v6
	v_mul_hi_u32 v3, v5, v3
	v_mul_lo_u32 v6, v3, s8
	v_sub_u32_e32 v5, v5, v6
	v_add_u32_e32 v6, 1, v3
	v_cmp_le_u32_e64 s[0:1], s8, v5
	s_nop 1
	v_cndmask_b32_e64 v3, v3, v6, s[0:1]
	v_subrev_u32_e32 v6, s8, v5
	v_cndmask_b32_e64 v5, v5, v6, s[0:1]
	v_add_u32_e32 v6, 1, v3
	v_cmp_le_u32_e64 s[0:1], s8, v5
	s_nop 1
	v_cndmask_b32_e64 v3, v3, v6, s[0:1]
	v_xor_b32_e32 v3, v3, v4
	v_sub_u32_e32 v3, v3, v4
	v_lshlrev_b32_e32 v4, 2, v3
	v_sub_u32_e32 v5, 32, v4
	v_min_i32_e32 v5, 4, v5
	v_sub_u32_e32 v6, 0, v5
	v_max_i32_e32 v5, v5, v6
	v_cvt_f32_u32_e32 v6, v5
	v_mul_lo_u32 v3, v3, s4
	v_sub_u32_e32 v2, v2, v3
	s_waitcnt lgkmcnt(2)
	v_sub_u32_e32 v7, 0, v2
	v_rcp_iflag_f32_e32 v6, v6
	v_ashrrev_i32_e32 v3, 31, v2
	v_max_i32_e32 v2, v2, v7
	v_sub_u32_e32 v7, 0, v5
	v_mul_f32_e32 v6, 0x4f7ffffe, v6
	v_cvt_u32_f32_e32 v6, v6
	v_mul_lo_u32 v7, v7, v6
	v_mul_hi_u32 v7, v6, v7
	v_add_u32_e32 v6, v6, v7
	v_mul_hi_u32 v6, v2, v6
	v_mul_lo_u32 v6, v6, v5
	v_sub_u32_e32 v2, v2, v6
	v_sub_u32_e32 v6, v2, v5
	v_cmp_ge_u32_e64 s[0:1], v2, v5
	s_nop 1
	v_cndmask_b32_e64 v2, v2, v6, s[0:1]
	v_sub_u32_e32 v6, v2, v5
	v_cmp_ge_u32_e64 s[0:1], v2, v5
	s_nop 1
	v_cndmask_b32_e64 v2, v2, v6, s[0:1]
	v_xor_b32_e32 v2, v2, v3
	v_sub_u32_e32 v2, v2, v3
	v_add_u32_e32 v37, v2, v4

.LBB0_293:
	v_readlane_b32 s26, v254, 0
	s_mov_b64 s[44:45], s[82:83]
	v_readlane_b32 s27, v254, 1
	v_mov_b32_e32 v1, v0
	s_ashr_i32 s27, s26, 31
	s_waitcnt vmcnt(0)
	s_cmp_lg_u32 s33, 0x100
	s_cbranch_scc1 .Lrst_hg1_slow
	v_cmp_gt_u32_e32 vcc, 0x100, v0
	s_and_saveexec_b64 s[0:1], vcc
	s_cbranch_execz .Lrst_hg1_done
	s_and_b32 s4, s26, 7
	s_lshl_b32 s4, s4, 2
	s_bfe_u32 s28, s26, 0x20003
	s_or_b32 s4, s4, s28
	s_lshl_b32 s4, s4, 15
	s_add_u32 s28, s82, 0x36300000
	s_addc_u32 s29, s83, 0
	s_add_u32 s28, s28, s4
	s_addc_u32 s29, s29, 0
	v_lshlrev_b32_e32 v2, 7, v0
	global_load_dwordx4 v[4:7], v2, s[28:29]
	global_load_dwordx4 v[8:11], v2, s[28:29] offset:16
	global_load_dwordx4 v[12:15], v2, s[28:29] offset:32
	global_load_dwordx4 v[16:19], v2, s[28:29] offset:48
	global_load_dwordx4 v[20:23], v2, s[28:29] offset:64
	global_load_dwordx4 v[24:27], v2, s[28:29] offset:80
	global_load_dwordx4 v[28:31], v2, s[28:29] offset:96
	global_load_dwordx4 v[32:35], v2, s[28:29] offset:112
	v_readlane_b32 s4, v255, 4
	v_mov_b32_e32 v36, 0x358637bd
	s_waitcnt vmcnt(0)
	v_pk_add_f32 v[4:5], v[4:5], v[8:9]
	v_pk_add_f32 v[6:7], v[6:7], v[10:11]
	v_pk_add_f32 v[12:13], v[12:13], v[16:17]
	v_pk_add_f32 v[14:15], v[14:15], v[18:19]
	v_pk_add_f32 v[20:21], v[20:21], v[24:25]
	v_pk_add_f32 v[22:23], v[22:23], v[26:27]
	v_pk_add_f32 v[28:29], v[28:29], v[32:33]
	v_pk_add_f32 v[30:31], v[30:31], v[34:35]
	v_pk_add_f32 v[4:5], v[4:5], v[12:13]
	v_pk_add_f32 v[6:7], v[6:7], v[14:15]
	v_pk_add_f32 v[20:21], v[20:21], v[28:29]
	v_pk_add_f32 v[22:23], v[22:23], v[30:31]
	v_pk_add_f32 v[4:5], v[4:5], v[20:21]
	v_pk_add_f32 v[6:7], v[6:7], v[22:23]
	s_nop 0
	v_add_f32_e32 v4, v5, v4
	v_add_f32_e32 v6, v6, v7
	v_add_f32_e32 v4, v4, v6
	v_fmamk_f32 v4, v4, 0x3a000000, v36
	v_rsq_f32_e32 v4, v4
	v_lshl_add_u32 v3, v0, 2, s4
	s_nop 0
	ds_write_b32 v3, v4
	ds_write_b32 v3, v4 offset:1024
	ds_write_b32 v3, v4 offset:2048
	ds_write_b32 v3, v4 offset:3072

.Lrst_hg1_slow:
	v_mov_b64_e32 v[2:3], s[26:27]
	v_ashrrev_i32_e32 v34, 8, v1
	v_mad_i64_i32 v[2:3], s[0:1], v34, s33, v[2:3]
	s_mov_b64 s[0:1], 0x400
	s_nop 0
	v_cmp_gt_i64_e32 vcc, s[0:1], v[2:3]
	v_mov_b32_e32 v37, 0
	s_and_saveexec_b64 s[28:29], vcc
	s_cbranch_execz .LBB0_299
	v_ashrrev_i32_e32 v3, 31, v2
	v_lshrrev_b32_e32 v3, 29, v3
	v_add_u32_e32 v3, v2, v3
	v_and_b32_e32 v4, -8, v3
	v_sub_u32_e32 v4, v2, v4
	v_cmp_lt_i32_e64 s[0:1], -1, v4
	s_and_saveexec_b64 s[4:5], s[0:1]
	s_xor_b64 s[0:1], exec, s[4:5]
	v_lshlrev_b32_e32 v2, 7, v4
	s_andn2_saveexec_b64 s[0:1], s[0:1]
	v_lshl_add_u32 v2, v4, 7, v4
	s_or_b64 exec, exec, s[0:1]
	v_ashrrev_i32_e32 v3, 3, v3
	v_add_u32_e32 v2, v2, v3
	v_ashrrev_i32_e32 v3, 31, v2
	v_lshrrev_b32_e32 v3, 25, v3
	v_add_u32_e32 v3, v2, v3
	v_ashrrev_i32_e32 v4, 7, v3
	v_lshlrev_b32_e32 v4, 2, v4
	v_sub_u32_e32 v5, 32, v4
	v_min_i32_e32 v5, 4, v5
	s_waitcnt lgkmcnt(3)
	v_sub_u32_e32 v6, 0, v5
	v_max_i32_e32 v5, v5, v6
	v_cvt_f32_u32_e32 v6, v5
	v_and_b32_e32 v3, 0xffffff80, v3
	v_sub_u32_e32 v2, v2, v3
	s_waitcnt lgkmcnt(2)
	v_sub_u32_e32 v7, 0, v2
	v_rcp_iflag_f32_e32 v6, v6
	v_ashrrev_i32_e32 v3, 31, v2
	v_max_i32_e32 v2, v2, v7
	v_sub_u32_e32 v7, 0, v5
	v_mul_f32_e32 v6, 0x4f7ffffe, v6
	v_cvt_u32_f32_e32 v6, v6
	v_mul_lo_u32 v7, v7, v6
	v_mul_hi_u32 v7, v6, v7
	v_add_u32_e32 v6, v6, v7
	v_mul_hi_u32 v6, v2, v6
	v_mul_lo_u32 v6, v6, v5
	v_sub_u32_e32 v2, v2, v6
	v_sub_u32_e32 v6, v2, v5
	v_cmp_ge_u32_e64 s[0:1], v2, v5
	s_nop 1
	v_cndmask_b32_e64 v2, v2, v6, s[0:1]
	v_sub_u32_e32 v6, v2, v5
	v_cmp_ge_u32_e64 s[0:1], v2, v5
	s_nop 1
	v_cndmask_b32_e64 v2, v2, v6, s[0:1]
	v_xor_b32_e32 v2, v2, v3
	v_sub_u32_e32 v2, v2, v3
	v_add_u32_e32 v37, v4, v2
